# step-3 unit: gate loads, row-piece loads and epilogue norm-weight loads batched
# baseline (speedup 1.0000x reference)
.LBB0_1152:
	s_and_b32 s63, s5, 3
	s_lshl_b32 s0, s12, 3
	s_lshl_b32 s5, s63, 1
	s_or_b32 s0, s5, s0
	s_mul_i32 s5, s0, 34
	s_sub_i32 s1, s1, s4
	s_add_i32 s0, s5, s4
	s_add_i32 s1, s5, s1
	s_add_i32 s54, s1, 34
	s_ashr_i32 s1, s0, 31
	s_lshl_b64 s[4:5], s[0:1], 2
	v_readlane_b32 s20, v249, 31
	v_readlane_b32 s21, v249, 32
	s_add_u32 s4, s20, s4
	s_addc_u32 s5, s21, s5
	s_ashr_i32 s55, s54, 31
	global_load_dword v1, v3, s[4:5]
	s_lshl_b64 s[4:5], s[54:55], 2
	s_add_u32 s4, s20, s4
	s_addc_u32 s5, s21, s5
	global_load_dword v207, v3, s[4:5]
	s_movk_i32 s4, 0xff
	v_cmp_lt_i32_e32 vcc, s4, v116
	s_and_saveexec_b64 s[4:5], vcc
	s_xor_b64 s[4:5], exec, s[4:5]
	v_lshrrev_b32_e32 v2, 4, v116
	v_and_b32_e32 v48, 0x7fffff8, v2
	s_or_saveexec_b64 s[4:5], s[4:5]
	v_and_b32_e32 v2, 0x7f, v116
	v_add_u32_e32 v4, s57, v2
	v_mad_i64_i32 v[4:5], s[36:37], v4, s17, 0
	v_lshl_add_u64 v[4:5], s[30:31], 0, v[4:5]
	s_xor_b64 exec, exec, s[4:5]
	s_cbranch_execz .LBB0_1156
	s_movk_i32 s12, 0x80
	v_cmp_gt_u32_e32 vcc, s12, v116
	v_mov_b32_e32 v6, s54
	v_mov_b32_e32 v7, s0
	s_mov_b64 s[20:21], 0x2200
	v_cndmask_b32_e32 v6, v6, v7, vcc
	v_lshl_add_u64 v[8:9], v[4:5], 0, s[20:21]
	v_lshl_or_b32 v6, v6, 7, v2
	v_readlane_b32 s20, v252, 55
	v_ashrrev_i32_e32 v7, 31, v6
	v_readlane_b32 s21, v252, 56
	s_mov_b32 s12, 0xbfb8aa3b
	v_mov_b32_e32 v20, 0x7f800000
	v_lshl_add_u64 v[6:7], v[6:7], 2, s[20:21]
	global_load_dword v7, v[6:7], off
	v_lshl_add_u32 v6, v116, 2, 0
	v_add_u32_e32 v29, 0x1ac00, v6
	v_mov_b32_e32 v223, 0x7f800000
	v_ashrrev_i32_e32 v21, 4, v116
	v_and_b32_e32 v48, -8, v21
	v_or_b32_e32 v10, s63, v48
	v_ashrrev_i32_e32 v11, 31, v10
	v_lshl_add_u64 v[12:13], v[10:11], 1, v[8:9]
	global_load_ushort v21, v[12:13], off
	v_lshl_add_u64 v[12:13], v[10:11], 2, s[52:53]
	global_load_dword v22, v[12:13], off
	v_or_b32_e32 v10, 4, v10
	v_ashrrev_i32_e32 v11, 31, v10
	v_lshl_add_u64 v[8:9], v[10:11], 1, v[8:9]
	global_load_ushort v23, v[8:9], off
	global_load_dword v24, v[12:13], off offset:16
	s_waitcnt vmcnt(0)
	ds_write_b32 v29, v7
	v_lshlrev_b32_e32 v21, 16, v21
	v_add_f32_e32 v7, v22, v21
	v_add_u32_e32 v11, 0x19800, v6
	ds_write_b32 v11, v7
	v_add_u32_e32 v6, 0x19c00, v6
	v_lshlrev_b32_e32 v7, 16, v23
	v_add_f32_e32 v8, v24, v7
	v_mul_f32_e64 v9, |v8|, s12
	v_fma_f32 v10, |v8|, s12, -v9
	s_mov_b32 s12, 0xb2a5705f
	v_rndne_f32_e32 v11, v9
	v_fma_f32 v10, |v8|, s12, v10
	v_sub_f32_e32 v9, v9, v11
	v_add_f32_e32 v9, v9, v10
	v_exp_f32_e32 v9, v9
	v_cvt_i32_f32_e32 v10, v11
	s_mov_b32 s12, 0x42ce8ed0
	v_cmp_ngt_f32_e64 vcc, |v8|, s12
	s_mov_b32 s12, 0xc2b17218
	v_ldexp_f32 v9, v9, v10
	v_cndmask_b32_e32 v9, 0, v9, vcc
	v_cmp_nlt_f32_e64 vcc, |v8|, s12
	v_min_f32_e32 v7, 0, v8
	s_mov_b32 s12, 0x3f2aaaab
	v_cndmask_b32_e32 v8, v20, v9, vcc
	v_add_f32_e32 v9, 1.0, v8
	v_add_f32_e32 v10, -1.0, v9
	v_sub_f32_e32 v11, v10, v9
	v_add_f32_e32 v11, 1.0, v11
	v_sub_f32_e32 v10, v8, v10
	v_add_f32_e32 v12, v10, v11
	v_frexp_mant_f32_e32 v10, v9
	v_cmp_gt_f32_e32 vcc, s12, v10
	v_cvt_f64_f32_e32 v[10:11], v9
	v_frexp_exp_i32_f64_e32 v10, v[10:11]
	v_subbrev_co_u32_e32 v10, vcc, 0, v10, vcc
	v_sub_u32_e32 v11, 0, v10
	v_ldexp_f32 v9, v9, v11
	v_ldexp_f32 v11, v12, v11
	v_add_f32_e32 v12, -1.0, v9
	v_add_f32_e32 v13, 1.0, v12
	v_sub_f32_e32 v13, v9, v13
	v_add_f32_e32 v13, v11, v13
	v_add_f32_e32 v14, v12, v13
	v_sub_f32_e32 v12, v12, v14
	v_add_f32_e32 v12, v13, v12
	v_add_f32_e32 v13, 1.0, v9
	v_add_f32_e32 v15, -1.0, v13
	v_sub_f32_e32 v9, v9, v15
	v_add_f32_e32 v9, v11, v9
	v_add_f32_e32 v11, v13, v9
	v_sub_f32_e32 v13, v13, v11
	v_add_f32_e32 v9, v9, v13
	v_rcp_f32_e32 v13, v11
	v_cvt_f32_i32_e32 v10, v10
	s_mov_b32 s12, 0x3f317218
	v_mul_f32_e32 v15, v14, v13
	v_mul_f32_e32 v16, v11, v15
	v_fma_f32 v17, v15, v11, -v16
	v_fmac_f32_e32 v17, v15, v9
	v_add_f32_e32 v18, v16, v17
	v_sub_f32_e32 v19, v14, v18
	v_sub_f32_e32 v14, v14, v19
	v_sub_f32_e32 v16, v18, v16
	v_sub_f32_e32 v14, v14, v18
	v_add_f32_e32 v12, v12, v14
	v_sub_f32_e32 v14, v16, v17
	v_add_f32_e32 v12, v14, v12
	v_add_f32_e32 v14, v19, v12
	v_mul_f32_e32 v16, v13, v14
	v_mul_f32_e32 v17, v11, v16
	v_fma_f32 v11, v16, v11, -v17
	v_fmac_f32_e32 v11, v16, v9
	v_sub_f32_e32 v9, v19, v14
	v_add_f32_e32 v9, v12, v9
	v_add_f32_e32 v12, v17, v11
	v_sub_f32_e32 v18, v14, v12
	v_sub_f32_e32 v14, v14, v18
	v_sub_f32_e32 v17, v12, v17
	v_sub_f32_e32 v12, v14, v12
	v_add_f32_e32 v9, v9, v12
	v_sub_f32_e32 v11, v17, v11
	v_add_f32_e32 v9, v11, v9
	v_add_f32_e32 v11, v15, v16
	v_add_f32_e32 v9, v18, v9
	v_sub_f32_e32 v12, v11, v15
	v_mul_f32_e32 v9, v13, v9
	v_sub_f32_e32 v12, v16, v12
	v_add_f32_e32 v9, v12, v9
	v_mul_f32_e32 v15, 0x3f317218, v10
	v_add_f32_e32 v12, v11, v9
	v_fma_f32 v16, v10, s12, -v15
	v_mul_f32_e32 v13, v12, v12
	v_mov_b32_e32 v14, 0x3ecc95a3
	v_fmac_f32_e32 v16, 0xb102e308, v10
	v_sub_f32_e32 v10, v12, v11
	v_fmamk_f32 v14, v13, 0x3e9b6dac, v14
	v_sub_f32_e32 v9, v9, v10
	v_add_f32_e32 v10, v15, v16
	v_fmaak_f32 v14, v13, v14, 0x3f2aaada
	v_sub_f32_e32 v11, v10, v15
	v_ldexp_f32 v15, v12, 1
	v_mul_f32_e32 v12, v12, v13
	v_mul_f32_e32 v12, v12, v14
	v_add_f32_e32 v13, v15, v12
	v_sub_f32_e32 v14, v13, v15
	v_ldexp_f32 v9, v9, 1
	v_sub_f32_e32 v12, v12, v14
	v_add_f32_e32 v9, v9, v12
	v_add_f32_e32 v12, v13, v9
	v_sub_f32_e32 v13, v12, v13
	v_sub_f32_e32 v9, v9, v13
	v_add_f32_e32 v13, v10, v12
	v_sub_f32_e32 v14, v13, v10
	v_sub_f32_e32 v15, v13, v14
	v_sub_f32_e32 v11, v16, v11
	v_sub_f32_e32 v10, v10, v15
	v_sub_f32_e32 v12, v12, v14
	v_add_f32_e32 v10, v12, v10
	v_add_f32_e32 v12, v11, v9
	v_sub_f32_e32 v14, v12, v11
	v_sub_f32_e32 v15, v12, v14
	v_sub_f32_e32 v11, v11, v15
	v_sub_f32_e32 v9, v9, v14
	v_add_f32_e32 v10, v12, v10
	v_add_f32_e32 v9, v9, v11
	v_add_f32_e32 v11, v13, v10
	v_sub_f32_e32 v12, v11, v13
	v_sub_f32_e32 v10, v10, v12
	v_add_f32_e32 v9, v9, v10
	s_mov_b32 s12, 0x7f800000
	v_add_f32_e32 v9, v11, v9
	v_cmp_neq_f32_e32 vcc, s12, v8
	s_mov_b32 s12, 0x33800000
	s_nop 0
	v_cndmask_b32_e32 v9, v20, v9, vcc
	v_cmp_lt_f32_e64 vcc, |v8|, s12
	s_nop 1
	v_cndmask_b32_e32 v8, v9, v8, vcc
	v_sub_f32_e32 v7, v7, v8
	ds_write_b32 v6, v7
.LBB0_1156:
	s_or_b64 exec, exec, s[4:5]
	s_lshl_b32 s12, s63, 8
	v_lshl_add_u64 v[4:5], v[4:5], 0, s[12:13]
	v_ashrrev_i32_e32 v49, 31, v48
	v_lshl_add_u64 v[6:7], v[48:49], 1, v[4:5]
	v_add_co_u32_e32 v40, vcc, 0x1000, v6
	v_add_u32_e32 v6, 0x200, v116
	v_ashrrev_i32_e32 v6, 4, v6
	v_and_b32_e32 v54, -8, v6
	v_ashrrev_i32_e32 v55, 31, v54
	v_addc_co_u32_e32 v41, vcc, 0, v7, vcc
	v_lshl_add_u64 v[6:7], v[54:55], 1, v[4:5]
	s_movk_i32 s4, 0x1000
	v_add_co_u32_e32 v36, vcc, s4, v6
	v_add_u32_e32 v6, 0x400, v116
	v_ashrrev_i32_e32 v6, 4, v6
	v_and_b32_e32 v52, -8, v6
	v_ashrrev_i32_e32 v53, 31, v52
	v_addc_co_u32_e32 v37, vcc, 0, v7, vcc
	v_lshl_add_u64 v[6:7], v[52:53], 1, v[4:5]
	v_add_co_u32_e32 v38, vcc, s4, v6
	v_add_u32_e32 v6, 0x600, v116
	v_ashrrev_i32_e32 v6, 4, v6
	v_and_b32_e32 v50, -8, v6
	global_load_dwordx4 v[28:31], v[40:41], off offset:512
	global_load_dwordx4 v[32:35], v[40:41], off offset:1536
	v_ashrrev_i32_e32 v51, 31, v50
	v_addc_co_u32_e32 v39, vcc, 0, v7, vcc
	v_lshl_add_u64 v[4:5], v[50:51], 1, v[4:5]
	v_add_co_u32_e32 v56, vcc, s4, v4
	global_load_dwordx4 v[20:23], v[36:37], off offset:512
	global_load_dwordx4 v[24:27], v[36:37], off offset:1536
	v_addc_co_u32_e32 v57, vcc, 0, v5, vcc
	global_load_dwordx4 v[12:15], v[38:39], off offset:512
	global_load_dwordx4 v[16:19], v[38:39], off offset:1536
	global_load_dwordx4 v[4:7], v[56:57], off offset:512
	global_load_dwordx4 v[8:11], v[56:57], off offset:1536
	global_load_dwordx4 v[58:61], v[40:41], off offset:2560
	global_load_dwordx4 v[62:65], v[36:37], off offset:2560
	global_load_dwordx4 v[66:69], v[38:39], off offset:2560
	global_load_dwordx4 v[70:73], v[56:57], off offset:2560
	s_mov_b32 s12, 0x3db504f3
	v_lshlrev_b32_e32 v49, 1, v2
	v_readlane_b32 s5, v255, 12
	s_movk_i32 s4, 0x110
	v_mul_u32_u24_e32 v2, 0x88, v2
	v_add_u32_e32 v51, s5, v49
	v_lshl_add_u32 v2, v2, 1, 0
	s_ashr_i32 s61, s62, 8
	s_lshl_b64 s[0:1], s[0:1], 15
	v_and_b32_e32 v148, 31, v116
	v_bfe_u32 v149, v116, 5, 1
	s_movk_i32 s20, 0x110
	s_waitcnt vmcnt(10)
	v_lshlrev_b32_e32 v42, 16, v32
	v_and_b32_e32 v43, 0xffff0000, v32
	v_pk_mul_f32 v[42:43], v[42:43], s[12:13] op_sel_hi:[1,0]
	v_lshlrev_b32_e32 v40, 16, v33
	v_and_b32_e32 v41, 0xffff0000, v33
	v_cvt_pk_bf16_f32 v32, v42, v43
	v_mul_lo_u32 v42, v48, s4
	v_pk_mul_f32 v[40:41], v[40:41], s[12:13] op_sel_hi:[1,0]
	v_add_u32_e32 v53, v51, v42
	v_add3_u32 v55, s5, v42, v49
	v_cvt_pk_bf16_f32 v33, v40, v41
	v_lshlrev_b32_e32 v40, 16, v34
	v_and_b32_e32 v41, 0xffff0000, v34
	s_waitcnt vmcnt(3)
	ds_write_b16 v53, v58
	ds_write_b16_d16_hi v55, v58 offset:272
	ds_write_b16 v53, v59 offset:544
	ds_write_b16_d16_hi v55, v59 offset:816
	v_pk_mul_f32 v[40:41], v[40:41], s[12:13] op_sel_hi:[1,0]
	ds_write_b16 v53, v60 offset:1088
	v_cvt_pk_bf16_f32 v34, v40, v41
	v_lshlrev_b32_e32 v56, 16, v35
	v_and_b32_e32 v57, 0xffff0000, v35
	v_pk_mul_f32 v[56:57], v[56:57], s[12:13] op_sel_hi:[1,0]
	v_lshl_add_u32 v48, v48, 1, v2
	ds_write_b16_d16_hi v55, v60 offset:1360
	v_cvt_pk_bf16_f32 v35, v56, v57
	ds_write_b16 v53, v61 offset:1632
	ds_write_b16_d16_hi v55, v61 offset:1904
	ds_write_b128 v48, v[28:31]
	ds_write_b128 v48, v[32:35] offset:34816
	v_lshlrev_b32_e32 v28, 16, v24
	v_and_b32_e32 v29, 0xffff0000, v24
	v_pk_mul_f32 v[28:29], v[28:29], s[12:13] op_sel_hi:[1,0]
	s_nop 0
	v_cvt_pk_bf16_f32 v24, v28, v29
	v_mul_lo_u32 v28, v54, s4
	v_add_u32_e32 v30, v51, v28
	v_add3_u32 v31, s5, v28, v49
	v_lshlrev_b32_e32 v28, 16, v25
	v_and_b32_e32 v29, 0xffff0000, v25
	v_pk_mul_f32 v[28:29], v[28:29], s[12:13] op_sel_hi:[1,0]
	s_waitcnt vmcnt(2)
	ds_write_b16 v30, v62
	v_cvt_pk_bf16_f32 v25, v28, v29
	v_lshlrev_b32_e32 v28, 16, v26
	v_and_b32_e32 v29, 0xffff0000, v26
	v_pk_mul_f32 v[28:29], v[28:29], s[12:13] op_sel_hi:[1,0]
	ds_write_b16_d16_hi v31, v62 offset:272
	v_cvt_pk_bf16_f32 v26, v28, v29
	v_lshlrev_b32_e32 v28, 16, v27
	v_and_b32_e32 v29, 0xffff0000, v27
	v_pk_mul_f32 v[28:29], v[28:29], s[12:13] op_sel_hi:[1,0]
	ds_write_b16 v30, v63 offset:544
	ds_write_b16_d16_hi v31, v63 offset:816
	v_cvt_pk_bf16_f32 v27, v28, v29
	v_lshl_add_u32 v28, v54, 1, v2
	ds_write_b16 v30, v64 offset:1088
	ds_write_b16_d16_hi v31, v64 offset:1360
	ds_write_b16 v30, v65 offset:1632
	ds_write_b16_d16_hi v31, v65 offset:1904
	ds_write_b128 v28, v[20:23]
	ds_write_b128 v28, v[24:27] offset:34816
	v_lshlrev_b32_e32 v20, 16, v16
	v_and_b32_e32 v21, 0xffff0000, v16
	v_pk_mul_f32 v[20:21], v[20:21], s[12:13] op_sel_hi:[1,0]
	s_nop 0
	v_cvt_pk_bf16_f32 v16, v20, v21
	v_mul_lo_u32 v20, v52, s4
	v_add_u32_e32 v22, v51, v20
	v_add3_u32 v23, s5, v20, v49
	v_lshlrev_b32_e32 v20, 16, v17
	v_and_b32_e32 v21, 0xffff0000, v17
	v_pk_mul_f32 v[20:21], v[20:21], s[12:13] op_sel_hi:[1,0]
	s_waitcnt vmcnt(1)
	ds_write_b16 v22, v66
	v_cvt_pk_bf16_f32 v17, v20, v21
	v_lshlrev_b32_e32 v20, 16, v18
	v_and_b32_e32 v21, 0xffff0000, v18
	v_pk_mul_f32 v[20:21], v[20:21], s[12:13] op_sel_hi:[1,0]
	ds_write_b16_d16_hi v23, v66 offset:272
	v_cvt_pk_bf16_f32 v18, v20, v21
	v_lshlrev_b32_e32 v20, 16, v19
	v_and_b32_e32 v21, 0xffff0000, v19
	v_pk_mul_f32 v[20:21], v[20:21], s[12:13] op_sel_hi:[1,0]
	ds_write_b16 v22, v67 offset:544
	ds_write_b16_d16_hi v23, v67 offset:816
	v_cvt_pk_bf16_f32 v19, v20, v21
	v_lshl_add_u32 v20, v52, 1, v2
	ds_write_b16 v22, v68 offset:1088
	ds_write_b16_d16_hi v23, v68 offset:1360
	ds_write_b16 v22, v69 offset:1632
	ds_write_b16_d16_hi v23, v69 offset:1904
	ds_write_b128 v20, v[12:15]
	ds_write_b128 v20, v[16:19] offset:34816
	v_lshlrev_b32_e32 v12, 16, v8
	v_and_b32_e32 v13, 0xffff0000, v8
	v_pk_mul_f32 v[12:13], v[12:13], s[12:13] op_sel_hi:[1,0]
	v_lshl_add_u32 v2, v50, 1, v2
	v_cvt_pk_bf16_f32 v8, v12, v13
	v_mul_lo_u32 v12, v50, s4
	v_add_u32_e32 v14, v51, v12
	v_add3_u32 v15, s5, v12, v49
	v_lshlrev_b32_e32 v12, 16, v9
	v_and_b32_e32 v13, 0xffff0000, v9
	v_pk_mul_f32 v[12:13], v[12:13], s[12:13] op_sel_hi:[1,0]
	v_readlane_b32 s4, v252, 53
	v_cvt_pk_bf16_f32 v9, v12, v13
	v_lshlrev_b32_e32 v12, 16, v10
	v_and_b32_e32 v13, 0xffff0000, v10
	v_pk_mul_f32 v[12:13], v[12:13], s[12:13] op_sel_hi:[1,0]
	v_readlane_b32 s5, v252, 54
	v_cvt_pk_bf16_f32 v10, v12, v13
	v_lshlrev_b32_e32 v12, 16, v11
	v_and_b32_e32 v13, 0xffff0000, v11
	s_add_u32 s0, s4, s0
	v_pk_mul_f32 v[12:13], v[12:13], s[12:13] op_sel_hi:[1,0]
	s_addc_u32 s1, s5, s1
	s_lshl_b32 s56, s61, 6
	s_waitcnt vmcnt(0)
	ds_write_b16 v14, v70
	ds_write_b16_d16_hi v15, v70 offset:272
	ds_write_b16 v14, v71 offset:544
	ds_write_b16_d16_hi v15, v71 offset:816
	ds_write_b16 v14, v72 offset:1088
	ds_write_b16_d16_hi v15, v72 offset:1360
	v_cvt_pk_bf16_f32 v11, v12, v13
	ds_write_b16 v14, v73 offset:1632
	ds_write_b16_d16_hi v15, v73 offset:1904
	ds_write_b128 v2, v[4:7]
	ds_write_b128 v2, v[8:11] offset:34816
	v_or_b32_e32 v4, s56, v148
	v_ashrrev_i32_e32 v5, 31, v4
	v_lshlrev_b64 v[6:7], 8, v[4:5]
	v_lshl_add_u64 v[6:7], s[0:1], 0, v[6:7]
	v_lshlrev_b32_e32 v2, 4, v149
	v_lshl_add_u64 v[6:7], v[6:7], 0, v[2:3]
	global_load_dwordx4 v[52:55], v[6:7], off
	global_load_dwordx4 v[56:59], v[6:7], off offset:32
	global_load_dwordx4 v[60:63], v[6:7], off offset:64
	global_load_dwordx4 v[64:67], v[6:7], off offset:96
	global_load_dwordx4 v[68:71], v[6:7], off offset:128
	global_load_dwordx4 v[72:75], v[6:7], off offset:160
	global_load_dwordx4 v[76:79], v[6:7], off offset:192
	global_load_dwordx4 v[80:83], v[6:7], off offset:224
	v_add_co_u32_e32 v6, vcc, s84, v6
	s_movk_i32 s0, 0x7f
	s_nop 0
	v_addc_co_u32_e32 v7, vcc, 0, v7, vcc
	global_load_dwordx4 v[84:87], v[6:7], off
	global_load_dwordx4 v[88:91], v[6:7], off offset:32
	global_load_dwordx4 v[92:95], v[6:7], off offset:64
	global_load_dwordx4 v[96:99], v[6:7], off offset:96
	global_load_dwordx4 v[100:103], v[6:7], off offset:128
	global_load_dwordx4 v[104:107], v[6:7], off offset:160
	global_load_dwordx4 v[108:111], v[6:7], off offset:192
	global_load_dwordx4 v[112:115], v[6:7], off offset:224
	v_cmp_lt_i32_e32 vcc, s0, v116
	s_waitcnt lgkmcnt(0)
	s_barrier
	s_and_saveexec_b64 s[0:1], vcc
	s_xor_b64 s[0:1], exec, s[0:1]
	v_mbcnt_hi_u32_b32 v229, -1, v221
	s_or_saveexec_b64 s[58:59], s[0:1]
	v_and_b32_e32 v226, 63, v116
	s_xor_b64 exec, exec, s[58:59]
	s_cbranch_execz .LBB0_1164
	v_and_b32_e32 v8, 64, v222
	v_add_u32_e32 v9, -1, v222
	v_cmp_lt_i32_e32 vcc, v9, v8
	s_lshr_b32 s12, s62, 6
	s_cmp_lt_u32 s62, 64
	v_cndmask_b32_e32 v9, v9, v222, vcc
	v_lshlrev_b32_e32 v10, 2, v9
	v_add_u32_e32 v9, -2, v222
	v_cmp_lt_i32_e32 vcc, v9, v8
	s_cselect_b64 s[0:1], -1, 0
	s_lshl_b32 s4, s12, 9
	v_cndmask_b32_e32 v9, v9, v222, vcc
	v_lshlrev_b32_e32 v11, 2, v9
	v_add_u32_e32 v9, -4, v222
	v_cmp_lt_i32_e32 vcc, v9, v8
	s_add_i32 s4, s4, 0
	v_lshl_add_u32 v6, v226, 3, s4
	v_cndmask_b32_e32 v9, v9, v222, vcc
	v_lshlrev_b32_e32 v12, 2, v9
	v_add_u32_e32 v9, -8, v222
	v_cmp_lt_i32_e32 vcc, v9, v8
	v_add_u32_e32 v7, 0x19c00, v6
	v_add_u32_e32 v17, 0x19800, v6
	v_cndmask_b32_e32 v9, v9, v222, vcc
	v_lshlrev_b32_e32 v13, 2, v9
	v_add_u32_e32 v9, -16, v222
	ds_read_b64 v[6:7], v7
	v_cmp_lt_i32_e32 vcc, v9, v8
	v_cmp_eq_u32_e64 s[36:37], 0, v226
	v_cmp_gt_u32_e64 s[38:39], 2, v226
	v_cndmask_b32_e32 v9, v9, v222, vcc
	v_lshlrev_b32_e32 v14, 2, v9
	v_subrev_u32_e32 v9, 32, v222
	v_cmp_lt_i32_e32 vcc, v9, v8
	v_cmp_gt_u32_e64 s[40:41], 4, v226
	v_cmp_gt_u32_e64 s[44:45], 8, v226
	v_cndmask_b32_e32 v8, v9, v222, vcc
	s_waitcnt lgkmcnt(0)
	v_add_f32_e32 v9, v6, v7
	ds_bpermute_b32 v18, v10, v9
	v_cmp_gt_u32_e64 s[46:47], 16, v226
	v_lshlrev_b32_e32 v15, 2, v8
	v_cmp_gt_u32_e64 s[48:49], 32, v226
	v_lshlrev_b32_e32 v16, 2, v222
	s_waitcnt lgkmcnt(0)
	v_add_f32_e32 v18, v9, v18
	v_cndmask_b32_e64 v9, v18, v9, s[36:37]
	ds_bpermute_b32 v18, v11, v9
	v_or_b32_e32 v8, 0xfc, v16
	s_cmp_gt_u32 s62, 63
	s_mov_b64 s[4:5], -1
	s_waitcnt lgkmcnt(0)
	v_add_f32_e32 v18, v9, v18
	v_cndmask_b32_e64 v9, v18, v9, s[38:39]
	ds_bpermute_b32 v18, v12, v9
	s_waitcnt lgkmcnt(0)
	v_add_f32_e32 v18, v9, v18
	v_cndmask_b32_e64 v9, v18, v9, s[40:41]
	ds_bpermute_b32 v18, v13, v9
	s_waitcnt lgkmcnt(0)
	v_add_f32_e32 v18, v9, v18
	v_cndmask_b32_e64 v9, v18, v9, s[44:45]
	ds_bpermute_b32 v18, v14, v9
	s_waitcnt lgkmcnt(0)
	v_add_f32_e32 v18, v9, v18
	v_cndmask_b32_e64 v9, v18, v9, s[46:47]
	ds_bpermute_b32 v18, v15, v9
	s_waitcnt lgkmcnt(0)
	v_add_f32_e32 v18, v9, v18
	v_cndmask_b32_e64 v9, v18, v9, s[48:49]
	ds_bpermute_b32 v18, v8, v9
	v_sub_f32_e32 v8, v9, v7
	s_waitcnt lgkmcnt(0)
	v_pk_add_f32 v[18:19], v[18:19], v[8:9] op_sel_hi:[0,1] neg_lo:[0,1] neg_hi:[0,1]
	v_pk_add_f32 v[6:7], v[6:7], v[18:19]
	s_nop 0
	v_cndmask_b32_e64 v7, v7, v9, s[0:1]
	v_cndmask_b32_e64 v6, v6, v8, s[0:1]
	ds_read_b64 v[8:9], v17
	s_waitcnt lgkmcnt(0)
	v_pk_add_f32 v[8:9], v[8:9], v[6:7] neg_lo:[0,1] neg_hi:[0,1]
	s_nop 0
	v_max_f32_e32 v17, v8, v9
	v_max_f32_e32 v18, v17, v17
	s_cbranch_scc0 .LBB0_1161
	v_and_b32_e32 v19, 63, v222
	v_cmp_ne_u32_e32 vcc, 63, v19
	v_cmp_gt_u32_e64 s[4:5], 62, v19
	v_or_b32_e32 v16, 0x80, v16
	v_addc_co_u32_e32 v20, vcc, 0, v222, vcc
	v_lshlrev_b32_e32 v21, 2, v20
	ds_bpermute_b32 v20, v21, v17
	v_cmp_eq_u32_e32 vcc, 63, v226
	v_cndmask_b32_e64 v22, 0, 2, s[4:5]
	v_add_lshl_u32 v22, v22, v222, 2
	v_cmp_gt_u32_e64 s[4:5], 62, v226
	s_waitcnt lgkmcnt(0)
	v_max_f32_e32 v20, v20, v20
	v_max_f32_e32 v20, v18, v20
	v_cndmask_b32_e32 v20, v20, v17, vcc
	ds_bpermute_b32 v22, v22, v20
	v_max_f32_e32 v23, v20, v20
	s_waitcnt lgkmcnt(0)
	v_max_f32_e32 v22, v22, v22
	v_max_f32_e32 v22, v23, v22
	v_cndmask_b32_e64 v20, v20, v22, s[4:5]
	v_cmp_gt_u32_e64 s[4:5], 60, v19
	v_max_f32_e32 v23, v20, v20
	s_nop 0
	v_cndmask_b32_e64 v22, 0, 4, s[4:5]
	v_add_lshl_u32 v22, v22, v222, 2
	ds_bpermute_b32 v22, v22, v20
	v_cmp_gt_u32_e64 s[4:5], 60, v226
	s_waitcnt lgkmcnt(0)
	v_max_f32_e32 v22, v22, v22
	v_max_f32_e32 v22, v23, v22
	v_cndmask_b32_e64 v20, v20, v22, s[4:5]
	v_cmp_gt_u32_e64 s[4:5], 56, v19
	v_max_f32_e32 v23, v20, v20
	s_nop 0
	v_cndmask_b32_e64 v22, 0, 8, s[4:5]
	v_add_lshl_u32 v22, v22, v222, 2
	ds_bpermute_b32 v22, v22, v20
	v_cmp_gt_u32_e64 s[4:5], 56, v226
	s_waitcnt lgkmcnt(0)
	v_max_f32_e32 v22, v22, v22
	v_max_f32_e32 v22, v23, v22
	v_cndmask_b32_e64 v20, v20, v22, s[4:5]
	v_cmp_gt_u32_e64 s[4:5], 48, v19
	v_max_f32_e32 v22, v20, v20
	s_nop 0
	v_cndmask_b32_e64 v19, 0, 16, s[4:5]
	v_add_lshl_u32 v19, v19, v222, 2
	ds_bpermute_b32 v19, v19, v20
	v_cmp_gt_u32_e64 s[4:5], 48, v226
	s_waitcnt lgkmcnt(0)
	v_max_f32_e32 v19, v19, v19
	v_max_f32_e32 v19, v22, v19
	v_cndmask_b32_e64 v19, v20, v19, s[4:5]
	ds_bpermute_b32 v16, v16, v19
	v_max_f32_e32 v20, v19, v19
	s_mov_b64 s[4:5], 0
	s_waitcnt lgkmcnt(0)
	v_max_f32_e32 v16, v16, v16
	v_max_f32_e32 v16, v20, v16
	v_cndmask_b32_e64 v20, v19, v16, s[48:49]
	ds_bpermute_b32 v16, v21, v20
	v_max_f32_e32 v19, v9, v9
	s_waitcnt lgkmcnt(0)
	v_max_f32_e32 v16, v16, v16
	v_max_f32_e32 v16, v16, v19
	v_cndmask_b32_e32 v19, v16, v9, vcc
